# attention finalize: 8 LDS read-backs issued together, stores with incremental addresses (one v_mul_lo_u32 instead of 8, no per-piece lgkmcnt(0))
# baseline (speedup 1.0000x reference)
.LBB0_740:
	s_or_b64 exec, exec, s[80:81]
	s_add_i32 s68, s68, s78
	v_lshlrev_b32_e32 v50, 2, v165
	v_and_b32_e32 v50, 12, v50
	v_xor_b32_e32 v50, v50, v164
	v_lshlrev_b32_e32 v51, 4, v50
	v_lshl_add_u32 v52, v165, 8, s71
	v_lshl_add_u32 v52, v164, 4, v52
	ds_read_b128 v[18:21], v52
	ds_read_b128 v[22:25], v52 offset:1024
	ds_read_b128 v[26:29], v52 offset:2048
	ds_read_b128 v[30:33], v52 offset:3072
	ds_read_b128 v[34:37], v52 offset:4096
	ds_read_b128 v[38:41], v52 offset:5120
	ds_read_b128 v[42:45], v52 offset:6144
	ds_read_b128 v[46:49], v52 offset:7168
	v_add_u32_e32 v53, s68, v165
	v_mul_lo_u32 v53, v53, s77
	v_add_u32_e32 v53, v53, v217
	s_lshl_b32 s80, s77, 2
	v_mov_b32_e32 v55, 0
	s_mov_b32 s81, 0
	v_add3_u32 v54, v51, v53, s81
	v_lshl_add_u64 v[56:57], v[150:151], 0, v[54:55]
	s_waitcnt lgkmcnt(7)
	global_store_dwordx4 v[56:57], v[18:21], off
	s_add_i32 s81, s81, s80
	v_xor_b32_e32 v54, 0x10, v51
	v_add3_u32 v54, v54, v53, s81
	v_lshl_add_u64 v[56:57], v[150:151], 0, v[54:55]
	s_waitcnt lgkmcnt(6)
	global_store_dwordx4 v[56:57], v[22:25], off
	s_add_i32 s81, s81, s80
	v_xor_b32_e32 v54, 0x20, v51
	v_add3_u32 v54, v54, v53, s81
	v_lshl_add_u64 v[56:57], v[150:151], 0, v[54:55]
	s_waitcnt lgkmcnt(5)
	global_store_dwordx4 v[56:57], v[26:29], off
	s_add_i32 s81, s81, s80
	v_xor_b32_e32 v54, 0x30, v51
	v_add3_u32 v54, v54, v53, s81
	v_lshl_add_u64 v[56:57], v[150:151], 0, v[54:55]
	s_waitcnt lgkmcnt(4)
	global_store_dwordx4 v[56:57], v[30:33], off
	s_add_i32 s81, s81, s80
	v_add3_u32 v54, v51, v53, s81
	v_lshl_add_u64 v[56:57], v[150:151], 0, v[54:55]
	s_waitcnt lgkmcnt(3)
	global_store_dwordx4 v[56:57], v[34:37], off
	s_add_i32 s81, s81, s80
	v_xor_b32_e32 v54, 0x10, v51
	v_add3_u32 v54, v54, v53, s81
	v_lshl_add_u64 v[56:57], v[150:151], 0, v[54:55]
	s_waitcnt lgkmcnt(2)
	global_store_dwordx4 v[56:57], v[38:41], off
	s_add_i32 s81, s81, s80
	v_xor_b32_e32 v54, 0x20, v51
	v_add3_u32 v54, v54, v53, s81
	v_lshl_add_u64 v[56:57], v[150:151], 0, v[54:55]
	s_waitcnt lgkmcnt(1)
	global_store_dwordx4 v[56:57], v[42:45], off
	s_add_i32 s81, s81, s80
	v_xor_b32_e32 v54, 0x30, v51
	v_add3_u32 v54, v54, v53, s81
	v_lshl_add_u64 v[56:57], v[150:151], 0, v[54:55]
	s_waitcnt lgkmcnt(0)
	global_store_dwordx4 v[56:57], v[46:49], off
	v_mov_b32_e32 v17, 0
	s_mov_b32 s78, 1
	v_mov_b32_e32 v231, 0xf149f2ca
	v_mov_b32_e32 v16, v17
	v_mov_b32_e32 v15, v17
	v_mov_b32_e32 v11, v17
	v_mov_b32_e32 v14, v17
	v_mov_b32_e32 v13, v17
	v_mov_b32_e32 v12, v17
	v_mov_b32_e32 v10, v17
	v_mov_b32_e32 v9, v17
	v_mov_b32_e32 v8, v17
	v_mov_b32_e32 v7, v17
	v_mov_b32_e32 v6, v17
	v_mov_b32_e32 v5, v17
	v_mov_b32_e32 v4, v17
	v_mov_b32_e32 v3, v17
	v_mov_b32_e32 v2, v17
	v_mov_b32_e32 v33, v17
	v_mov_b32_e32 v32, v17
	v_mov_b32_e32 v31, v17
	v_mov_b32_e32 v30, v17
	v_mov_b32_e32 v29, v17
	v_mov_b32_e32 v28, v17
	v_mov_b32_e32 v27, v17
	v_mov_b32_e32 v26, v17
	v_mov_b32_e32 v25, v17
	v_mov_b32_e32 v24, v17
	v_mov_b32_e32 v23, v17
	v_mov_b32_e32 v22, v17
	v_mov_b32_e32 v21, v17
	v_mov_b32_e32 v20, v17
	v_mov_b32_e32 v19, v17
	v_mov_b32_e32 v18, v17
	v_mov_b32_e32 v65, v17
	v_mov_b32_e32 v64, v17
	v_mov_b32_e32 v63, v17
	v_mov_b32_e32 v62, v17
	v_mov_b32_e32 v61, v17
	v_mov_b32_e32 v60, v17
	v_mov_b32_e32 v59, v17
	v_mov_b32_e32 v58, v17
	v_mov_b32_e32 v57, v17
	v_mov_b32_e32 v56, v17
	v_mov_b32_e32 v55, v17
	v_mov_b32_e32 v54, v17
	v_mov_b32_e32 v53, v17
	v_mov_b32_e32 v52, v17
	v_mov_b32_e32 v51, v17
	v_mov_b32_e32 v50, v17
	v_mov_b32_e32 v49, v17
	v_mov_b32_e32 v48, v17
	v_mov_b32_e32 v47, v17
	v_mov_b32_e32 v46, v17
	v_mov_b32_e32 v45, v17
	v_mov_b32_e32 v44, v17
	v_mov_b32_e32 v43, v17
	v_mov_b32_e32 v42, v17
	v_mov_b32_e32 v41, v17
	v_mov_b32_e32 v40, v17
	v_mov_b32_e32 v39, v17
	v_mov_b32_e32 v38, v17
	v_mov_b32_e32 v37, v17
	v_mov_b32_e32 v36, v17
	v_mov_b32_e32 v35, v17
	v_mov_b32_e32 v34, v17
	v_mov_b32_e32 v232, v17
	s_mov_b32 s73, s84

.LBB0_810:
	s_or_b64 exec, exec, s[80:81]
	v_lshlrev_b32_e32 v50, 2, v165
	v_and_b32_e32 v50, 12, v50
	v_xor_b32_e32 v50, v50, v164
	v_lshlrev_b32_e32 v51, 4, v50
	v_lshl_add_u32 v52, v165, 8, s71
	v_lshl_add_u32 v52, v164, 4, v52
	ds_read_b128 v[18:21], v52
	ds_read_b128 v[22:25], v52 offset:1024
	ds_read_b128 v[26:29], v52 offset:2048
	ds_read_b128 v[30:33], v52 offset:3072
	ds_read_b128 v[34:37], v52 offset:4096
	ds_read_b128 v[38:41], v52 offset:5120
	ds_read_b128 v[42:45], v52 offset:6144
	ds_read_b128 v[46:49], v52 offset:7168
	v_add_u32_e32 v53, s73, v165
	v_lshl_add_u32 v53, v53, 2, s78
	v_mul_lo_u32 v53, v53, s77
	v_add_u32_e32 v53, v53, v218
	s_lshl_b32 s80, s77, 4
	v_mov_b32_e32 v55, 0
	s_mov_b32 s81, 0
	v_add3_u32 v54, v51, v53, s81
	v_lshl_add_u64 v[56:57], v[150:151], 0, v[54:55]
	s_waitcnt lgkmcnt(7)
	global_store_dwordx4 v[56:57], v[18:21], off
	s_add_i32 s81, s81, s80
	v_xor_b32_e32 v54, 0x10, v51
	v_add3_u32 v54, v54, v53, s81
	v_lshl_add_u64 v[56:57], v[150:151], 0, v[54:55]
	s_waitcnt lgkmcnt(6)
	global_store_dwordx4 v[56:57], v[22:25], off
	s_add_i32 s81, s81, s80
	v_xor_b32_e32 v54, 0x20, v51
	v_add3_u32 v54, v54, v53, s81
	v_lshl_add_u64 v[56:57], v[150:151], 0, v[54:55]
	s_waitcnt lgkmcnt(5)
	global_store_dwordx4 v[56:57], v[26:29], off
	s_add_i32 s81, s81, s80
	v_xor_b32_e32 v54, 0x30, v51
	v_add3_u32 v54, v54, v53, s81
	v_lshl_add_u64 v[56:57], v[150:151], 0, v[54:55]
	s_waitcnt lgkmcnt(4)
	global_store_dwordx4 v[56:57], v[30:33], off
	s_add_i32 s81, s81, s80
	v_add3_u32 v54, v51, v53, s81
	v_lshl_add_u64 v[56:57], v[150:151], 0, v[54:55]
	s_waitcnt lgkmcnt(3)
	global_store_dwordx4 v[56:57], v[34:37], off
	s_add_i32 s81, s81, s80
	v_xor_b32_e32 v54, 0x10, v51
	v_add3_u32 v54, v54, v53, s81
	v_lshl_add_u64 v[56:57], v[150:151], 0, v[54:55]
	s_waitcnt lgkmcnt(2)
	global_store_dwordx4 v[56:57], v[38:41], off
	s_add_i32 s81, s81, s80
	v_xor_b32_e32 v54, 0x20, v51
	v_add3_u32 v54, v54, v53, s81
	v_lshl_add_u64 v[56:57], v[150:151], 0, v[54:55]
	s_waitcnt lgkmcnt(1)
	global_store_dwordx4 v[56:57], v[42:45], off
	s_add_i32 s81, s81, s80
	v_xor_b32_e32 v54, 0x30, v51
	v_add3_u32 v54, v54, v53, s81
	v_lshl_add_u64 v[56:57], v[150:151], 0, v[54:55]
	s_waitcnt lgkmcnt(0)
	global_store_dwordx4 v[56:57], v[46:49], off
	v_mov_b32_e32 v17, 0
	v_mov_b32_e32 v233, 0xf149f2ca
	v_mov_b32_e32 v16, v17
	v_mov_b32_e32 v33, v17
	v_mov_b32_e32 v15, v17
	v_mov_b32_e32 v11, v17
	s_mov_b32 s78, 1
	v_mov_b32_e32 v14, v17
	v_mov_b32_e32 v13, v17
	v_mov_b32_e32 v12, v17
	v_mov_b32_e32 v10, v17
	v_mov_b32_e32 v9, v17
	v_mov_b32_e32 v8, v17
	v_mov_b32_e32 v7, v17
	v_mov_b32_e32 v6, v17
	v_mov_b32_e32 v5, v17
	v_mov_b32_e32 v4, v17
	v_mov_b32_e32 v3, v17
	v_mov_b32_e32 v2, v17
	v_mov_b32_e32 v32, v17
	v_mov_b32_e32 v31, v17
	v_mov_b32_e32 v30, v17
	v_mov_b32_e32 v29, v17
	v_mov_b32_e32 v28, v17
	v_mov_b32_e32 v27, v17
	v_mov_b32_e32 v26, v17
	v_mov_b32_e32 v25, v17
	v_mov_b32_e32 v24, v17
	v_mov_b32_e32 v23, v17
	v_mov_b32_e32 v22, v17
	v_mov_b32_e32 v21, v17
	v_mov_b32_e32 v20, v17
	v_mov_b32_e32 v19, v17
	v_mov_b32_e32 v18, v17
	v_mov_b32_e32 v65, v17
	v_mov_b32_e32 v64, v17
	v_mov_b32_e32 v63, v17
	v_mov_b32_e32 v62, v17
	v_mov_b32_e32 v61, v17
	v_mov_b32_e32 v60, v17
	v_mov_b32_e32 v59, v17
	v_mov_b32_e32 v58, v17
	v_mov_b32_e32 v57, v17
	v_mov_b32_e32 v56, v17
	v_mov_b32_e32 v55, v17
	v_mov_b32_e32 v54, v17
	v_mov_b32_e32 v53, v17
	v_mov_b32_e32 v52, v17
	v_mov_b32_e32 v51, v17
	v_mov_b32_e32 v50, v17
	v_mov_b32_e32 v49, v17
	v_mov_b32_e32 v48, v17
	v_mov_b32_e32 v47, v17
	v_mov_b32_e32 v46, v17
	v_mov_b32_e32 v45, v17
	v_mov_b32_e32 v44, v17
	v_mov_b32_e32 v43, v17
	v_mov_b32_e32 v42, v17
	v_mov_b32_e32 v41, v17
	v_mov_b32_e32 v40, v17
	v_mov_b32_e32 v39, v17
	v_mov_b32_e32 v38, v17
	v_mov_b32_e32 v37, v17
	v_mov_b32_e32 v36, v17
	v_mov_b32_e32 v35, v17
	v_mov_b32_e32 v34, v17
	v_mov_b32_e32 v234, v17
	s_mov_b32 s73, s84

.LBB0_880:
	s_or_b64 exec, exec, s[80:81]
	s_lshl_b32 s68, s79, 8
	v_lshlrev_b32_e32 v50, 2, v165
	v_and_b32_e32 v50, 12, v50
	v_xor_b32_e32 v50, v50, v164
	v_lshlrev_b32_e32 v51, 4, v50
	v_lshl_add_u32 v52, v165, 8, s71
	v_lshl_add_u32 v52, v164, 4, v52
	ds_read_b128 v[18:21], v52
	ds_read_b128 v[22:25], v52 offset:1024
	ds_read_b128 v[26:29], v52 offset:2048
	ds_read_b128 v[30:33], v52 offset:3072
	ds_read_b128 v[34:37], v52 offset:4096
	ds_read_b128 v[38:41], v52 offset:5120
	ds_read_b128 v[42:45], v52 offset:6144
	ds_read_b128 v[46:49], v52 offset:7168
	v_add_u32_e32 v53, s78, v165
	v_lshl_add_u32 v53, v53, 12, s68
	s_movk_i32 s80, 0x4000
	v_mov_b32_e32 v55, 0
	s_mov_b32 s81, 0
	v_add3_u32 v54, v51, v53, s81
	v_lshl_add_u64 v[56:57], v[160:161], 0, v[54:55]
	s_waitcnt lgkmcnt(7)
	global_store_dwordx4 v[56:57], v[18:21], off
	s_add_i32 s81, s81, s80
	v_xor_b32_e32 v54, 0x10, v51
	v_add3_u32 v54, v54, v53, s81
	v_lshl_add_u64 v[56:57], v[160:161], 0, v[54:55]
	s_waitcnt lgkmcnt(6)
	global_store_dwordx4 v[56:57], v[22:25], off
	s_add_i32 s81, s81, s80
	v_xor_b32_e32 v54, 0x20, v51
	v_add3_u32 v54, v54, v53, s81
	v_lshl_add_u64 v[56:57], v[160:161], 0, v[54:55]
	s_waitcnt lgkmcnt(5)
	global_store_dwordx4 v[56:57], v[26:29], off
	s_add_i32 s81, s81, s80
	v_xor_b32_e32 v54, 0x30, v51
	v_add3_u32 v54, v54, v53, s81
	v_lshl_add_u64 v[56:57], v[160:161], 0, v[54:55]
	s_waitcnt lgkmcnt(4)
	global_store_dwordx4 v[56:57], v[30:33], off
	s_add_i32 s81, s81, s80
	v_add3_u32 v54, v51, v53, s81
	v_lshl_add_u64 v[56:57], v[160:161], 0, v[54:55]
	s_waitcnt lgkmcnt(3)
	global_store_dwordx4 v[56:57], v[34:37], off
	s_add_i32 s81, s81, s80
	v_xor_b32_e32 v54, 0x10, v51
	v_add3_u32 v54, v54, v53, s81
	v_lshl_add_u64 v[56:57], v[160:161], 0, v[54:55]
	s_waitcnt lgkmcnt(2)
	global_store_dwordx4 v[56:57], v[38:41], off
	s_add_i32 s81, s81, s80
	v_xor_b32_e32 v54, 0x20, v51
	v_add3_u32 v54, v54, v53, s81
	v_lshl_add_u64 v[56:57], v[160:161], 0, v[54:55]
	s_waitcnt lgkmcnt(1)
	global_store_dwordx4 v[56:57], v[42:45], off
	s_add_i32 s81, s81, s80
	v_xor_b32_e32 v54, 0x30, v51
	v_add3_u32 v54, v54, v53, s81
	v_lshl_add_u64 v[56:57], v[160:161], 0, v[54:55]
	s_waitcnt lgkmcnt(0)
	global_store_dwordx4 v[56:57], v[46:49], off
	v_mov_b32_e32 v17, 0
	s_mov_b32 s79, 1
	v_mov_b32_e32 v233, 0xf149f2ca
	v_mov_b32_e32 v16, v17
	v_mov_b32_e32 v15, v17
	v_mov_b32_e32 v11, v17
	v_mov_b32_e32 v14, v17
	v_mov_b32_e32 v13, v17
	v_mov_b32_e32 v12, v17
	v_mov_b32_e32 v10, v17
	v_mov_b32_e32 v9, v17
	v_mov_b32_e32 v8, v17
	v_mov_b32_e32 v7, v17
	v_mov_b32_e32 v6, v17
	v_mov_b32_e32 v5, v17
	v_mov_b32_e32 v4, v17
	v_mov_b32_e32 v3, v17
	v_mov_b32_e32 v2, v17
	v_mov_b32_e32 v33, v17
	v_mov_b32_e32 v32, v17
	v_mov_b32_e32 v31, v17
	v_mov_b32_e32 v30, v17
	v_mov_b32_e32 v29, v17
	v_mov_b32_e32 v28, v17
	v_mov_b32_e32 v27, v17
	v_mov_b32_e32 v26, v17
	v_mov_b32_e32 v25, v17
	v_mov_b32_e32 v24, v17
	v_mov_b32_e32 v23, v17
	v_mov_b32_e32 v22, v17
	v_mov_b32_e32 v21, v17
	v_mov_b32_e32 v20, v17
	v_mov_b32_e32 v19, v17
	v_mov_b32_e32 v18, v17
	v_mov_b32_e32 v65, v17
	v_mov_b32_e32 v64, v17
	v_mov_b32_e32 v63, v17
	v_mov_b32_e32 v62, v17
	v_mov_b32_e32 v61, v17
	v_mov_b32_e32 v60, v17
	v_mov_b32_e32 v59, v17
	v_mov_b32_e32 v58, v17
	v_mov_b32_e32 v57, v17
	v_mov_b32_e32 v56, v17
	v_mov_b32_e32 v55, v17
	v_mov_b32_e32 v54, v17
	v_mov_b32_e32 v53, v17
	v_mov_b32_e32 v52, v17
	v_mov_b32_e32 v51, v17
	v_mov_b32_e32 v50, v17
	v_mov_b32_e32 v49, v17
	v_mov_b32_e32 v48, v17
	v_mov_b32_e32 v47, v17
	v_mov_b32_e32 v46, v17
	v_mov_b32_e32 v45, v17
	v_mov_b32_e32 v44, v17
	v_mov_b32_e32 v43, v17
	v_mov_b32_e32 v42, v17
	v_mov_b32_e32 v41, v17
	v_mov_b32_e32 v40, v17
	v_mov_b32_e32 v39, v17
	v_mov_b32_e32 v38, v17
	v_mov_b32_e32 v37, v17
	v_mov_b32_e32 v36, v17
	v_mov_b32_e32 v35, v17
	v_mov_b32_e32 v34, v17
	v_mov_b32_e32 v234, v17
	s_mov_b32 s68, s84
